# baseline (speedup 1.0000x reference)
.LBB1_3:
	s_or_b64 exec, exec, s[4:5]
	v_mov_b32_e32 v14, 0
	v_mov_b32_e32 v15, 0
	v_mov_b32_e32 v16, 0
	v_mov_b32_e32 v17, 0
	v_mov_b32_e32 v18, 0
	v_mov_b32_e32 v19, 0
	v_mov_b32_e32 v20, 0
	v_mov_b32_e32 v21, 0
	s_and_saveexec_b64 s[4:5], vcc
	s_cbranch_execz .LBB1_5
	v_mov_b32_e32 v5, 0
	v_lshl_add_u64 v[0:1], v[2:3], 0, v[4:5]
	global_load_dwordx4 v[14:17], v[0:1], off offset:128
	global_load_dwordx4 v[18:21], v[0:1], off offset:144

.LBB1_34:
	s_or_b64 exec, exec, s[6:7]
	v_or_b32_e32 v119, 0x400, v244
	s_movk_i32 s6, 0x680
	v_cmp_gt_u32_e64 s[6:7], s6, v119
	v_mov_b32_e32 v133, 0
	v_mov_b32_e32 v134, 0
	v_mov_b32_e32 v135, 0
	s_and_saveexec_b64 s[8:9], s[6:7]
	s_cbranch_execz .LBB1_36
	v_lshlrev_b32_e32 v0, 4, v119
	global_load_dwordx4 v[132:135], v0, s[2:3]

.LBB1_63:
	s_or_b64 exec, exec, s[6:7]
	s_load_dwordx4 s[4:7], s[0:1], 0x78
	v_lshrrev_b32_e32 v111, 2, v244
	v_lshlrev_b32_e32 v113, 4, v170
	v_and_b32_e32 v181, 12, v111
	v_or_b32_e32 v1, v113, v181
	v_lshlrev_b32_e32 v1, 2, v1
	v_or_b32_e32 v175, v113, v183
	s_waitcnt lgkmcnt(0)
	s_barrier
	v_mov_b32_e32 v0, 0
	v_lshlrev_b32_e32 v110, 2, v175
	global_load_dwordx4 a[138:141], v1, s[4:5]
	global_load_dword v112, v110, s[4:5]
	global_load_dword a142, v0, s[6:7]
	ds_read_b64 v[0:1], v0 offset:34816
	s_waitcnt lgkmcnt(0)
	v_readfirstlane_b32 s6, v0
	v_readfirstlane_b32 s7, v1
	s_and_saveexec_b64 s[4:5], s[12:13]
	s_cbranch_execz .LBB1_70
	v_cmp_eq_u32_e32 vcc, 12, v183
	ds_read_b128 v[144:147], v124 offset:34832
	ds_read_b128 v[148:151], v124 offset:48144
	ds_read_b128 v[152:155], v124 offset:35856
	ds_read_b128 v[156:159], v124 offset:49168
	v_lshrrev_b32_e32 v114, 4, v244
	v_cndmask_b32_e64 v0, 0, 1.0, vcc
	v_pk_add_f32 v[2:3], v[0:1], v[6:7] op_sel_hi:[0,1]
	v_cvt_pk_f16_f32 v6, v2, v3
	v_pk_add_f32 v[2:3], v[0:1], v[8:9] op_sel_hi:[0,1]
	v_cvt_pk_f16_f32 v7, v2, v3
	v_pk_add_f32 v[2:3], v[0:1], v[10:11] op_sel_hi:[0,1]
	v_cvt_pk_f16_f32 v8, v2, v3
	v_pk_add_f32 v[2:3], v[0:1], v[12:13] op_sel_hi:[0,1]
	v_cvt_pk_f16_f32 v9, v2, v3
	v_pk_add_f32 v[2:3], v[0:1], v[14:15] op_sel_hi:[0,1]
	s_nop 0
	s_waitcnt lgkmcnt(3)
	v_mfma_f32_16x16x32_f16 a[0:3], v[6:9], v[144:147], 0
	ds_read_b128 v[144:147], v124 offset:36880
	s_movk_i32 s2, 0x190
	s_nop 0
	s_waitcnt lgkmcnt(3)
	v_mfma_f32_16x16x32_f16 a[4:7], v[6:9], v[148:151], 0
	ds_read_b128 v[148:151], v124 offset:50192
	v_cvt_pk_f16_f32 v6, v2, v3
	v_pk_add_f32 v[2:3], v[0:1], v[16:17] op_sel_hi:[0,1]
	v_cvt_pk_f16_f32 v7, v2, v3
	v_pk_add_f32 v[2:3], v[0:1], v[18:19] op_sel_hi:[0,1]
	v_cvt_pk_f16_f32 v8, v2, v3
	v_pk_add_f32 v[2:3], v[0:1], v[20:21] op_sel_hi:[0,1]
	v_cvt_pk_f16_f32 v9, v2, v3
	s_nop 0
	s_waitcnt lgkmcnt(3)
	v_mfma_f32_16x16x32_f16 a[0:3], v[6:9], v[152:155], a[0:3]
	ds_read_b128 v[152:155], v124 offset:37904
	v_pk_add_f32 v[2:3], v[0:1], v[26:27] op_sel_hi:[0,1]
	s_nop 0
	s_waitcnt lgkmcnt(3)
	v_mfma_f32_16x16x32_f16 a[4:7], v[6:9], v[156:159], a[4:7]
	ds_read_b128 v[156:159], v124 offset:51216
	v_cvt_pk_f16_f32 v6, v2, v3
	v_pk_add_f32 v[2:3], v[0:1], v[28:29] op_sel_hi:[0,1]
	v_cvt_pk_f16_f32 v7, v2, v3
	v_pk_add_f32 v[2:3], v[0:1], v[30:31] op_sel_hi:[0,1]
	v_cvt_pk_f16_f32 v8, v2, v3
	v_pk_add_f32 v[2:3], v[0:1], v[32:33] op_sel_hi:[0,1]
	v_cvt_pk_f16_f32 v9, v2, v3
	v_pk_add_f32 v[2:3], v[0:1], v[22:23] op_sel_hi:[0,1]
	s_nop 0
	s_waitcnt lgkmcnt(3)
	v_mfma_f32_16x16x32_f16 a[0:3], v[6:9], v[144:147], a[0:3]
	ds_read_b128 v[144:147], v124 offset:38928
	s_nop 0
	s_waitcnt lgkmcnt(3)
	v_mfma_f32_16x16x32_f16 a[4:7], v[6:9], v[148:151], a[4:7]
	ds_read_b128 v[148:151], v124 offset:52240
	v_cvt_pk_f16_f32 v6, v2, v3
	v_pk_add_f32 v[2:3], v[0:1], v[24:25] op_sel_hi:[0,1]
	v_cvt_pk_f16_f32 v7, v2, v3
	v_pk_add_f32 v[2:3], v[0:1], v[34:35] op_sel_hi:[0,1]
	v_cvt_pk_f16_f32 v8, v2, v3
	v_pk_add_f32 v[2:3], v[0:1], v[36:37] op_sel_hi:[0,1]
	v_cvt_pk_f16_f32 v9, v2, v3
	v_pk_add_f32 v[2:3], v[0:1], v[42:43] op_sel_hi:[0,1]
	s_nop 0
	s_waitcnt lgkmcnt(3)
	v_mfma_f32_16x16x32_f16 a[0:3], v[6:9], v[152:155], a[0:3]
	ds_read_b128 v[152:155], v124 offset:39952
	s_nop 0
	s_waitcnt lgkmcnt(3)
	v_mfma_f32_16x16x32_f16 a[4:7], v[6:9], v[156:159], a[4:7]
	ds_read_b128 v[156:159], v124 offset:53264
	v_cvt_pk_f16_f32 v6, v2, v3
	v_pk_add_f32 v[2:3], v[0:1], v[44:45] op_sel_hi:[0,1]
	v_cvt_pk_f16_f32 v7, v2, v3
	v_pk_add_f32 v[2:3], v[0:1], v[46:47] op_sel_hi:[0,1]
	v_cvt_pk_f16_f32 v8, v2, v3
	v_pk_add_f32 v[2:3], v[0:1], v[48:49] op_sel_hi:[0,1]
	v_cvt_pk_f16_f32 v9, v2, v3
	v_pk_add_f32 v[2:3], v[0:1], v[38:39] op_sel_hi:[0,1]
	s_nop 0
	s_waitcnt lgkmcnt(3)
	v_mfma_f32_16x16x32_f16 a[0:3], v[6:9], v[144:147], a[0:3]
	ds_read_b128 v[144:147], v124 offset:40976
	s_nop 0
	s_waitcnt lgkmcnt(3)
	v_mfma_f32_16x16x32_f16 a[4:7], v[6:9], v[148:151], a[4:7]
	ds_read_b128 v[148:151], v124 offset:54288
	v_cvt_pk_f16_f32 v6, v2, v3
	v_pk_add_f32 v[2:3], v[0:1], v[40:41] op_sel_hi:[0,1]
	v_cvt_pk_f16_f32 v7, v2, v3
	v_pk_add_f32 v[2:3], v[0:1], v[50:51] op_sel_hi:[0,1]
	v_cvt_pk_f16_f32 v8, v2, v3
	v_pk_add_f32 v[2:3], v[0:1], v[52:53] op_sel_hi:[0,1]
	v_cvt_pk_f16_f32 v9, v2, v3
	v_pk_add_f32 v[2:3], v[0:1], v[58:59] op_sel_hi:[0,1]
	s_nop 0
	s_waitcnt lgkmcnt(3)
	v_mfma_f32_16x16x32_f16 a[0:3], v[6:9], v[152:155], a[0:3]
	ds_read_b128 v[152:155], v124 offset:42000
	s_nop 0
	s_waitcnt lgkmcnt(3)
	v_mfma_f32_16x16x32_f16 a[4:7], v[6:9], v[156:159], a[4:7]
	ds_read_b128 v[156:159], v124 offset:55312
	v_cvt_pk_f16_f32 v6, v2, v3
	v_pk_add_f32 v[2:3], v[0:1], v[60:61] op_sel_hi:[0,1]
	v_cvt_pk_f16_f32 v7, v2, v3
	v_pk_add_f32 v[2:3], v[0:1], v[62:63] op_sel_hi:[0,1]
	v_cvt_pk_f16_f32 v8, v2, v3
	v_pk_add_f32 v[2:3], v[0:1], v[64:65] op_sel_hi:[0,1]
	v_cvt_pk_f16_f32 v9, v2, v3
	v_pk_add_f32 v[2:3], v[0:1], v[54:55] op_sel_hi:[0,1]
	s_nop 0
	s_waitcnt lgkmcnt(3)
	v_mfma_f32_16x16x32_f16 a[0:3], v[6:9], v[144:147], a[0:3]
	ds_read_b128 v[144:147], v124 offset:43024
	s_nop 0
	s_waitcnt lgkmcnt(3)
	v_mfma_f32_16x16x32_f16 a[4:7], v[6:9], v[148:151], a[4:7]
	ds_read_b128 v[148:151], v124 offset:56336
	v_cvt_pk_f16_f32 v6, v2, v3
	v_pk_add_f32 v[2:3], v[0:1], v[56:57] op_sel_hi:[0,1]
	v_cvt_pk_f16_f32 v7, v2, v3
	v_pk_add_f32 v[2:3], v[0:1], v[66:67] op_sel_hi:[0,1]
	v_cvt_pk_f16_f32 v8, v2, v3
	v_pk_add_f32 v[2:3], v[0:1], v[68:69] op_sel_hi:[0,1]
	v_cvt_pk_f16_f32 v9, v2, v3
	v_pk_add_f32 v[2:3], v[0:1], v[74:75] op_sel_hi:[0,1]
	s_nop 0
	s_waitcnt lgkmcnt(3)
	v_mfma_f32_16x16x32_f16 a[0:3], v[6:9], v[152:155], a[0:3]
	ds_read_b128 v[152:155], v124 offset:44048
	s_nop 0
	s_waitcnt lgkmcnt(3)
	v_mfma_f32_16x16x32_f16 a[4:7], v[6:9], v[156:159], a[4:7]
	ds_read_b128 v[156:159], v124 offset:57360
	v_cvt_pk_f16_f32 v6, v2, v3
	v_pk_add_f32 v[2:3], v[0:1], v[76:77] op_sel_hi:[0,1]
	v_cvt_pk_f16_f32 v7, v2, v3
	v_pk_add_f32 v[2:3], v[0:1], v[78:79] op_sel_hi:[0,1]
	v_cvt_pk_f16_f32 v8, v2, v3
	v_pk_add_f32 v[2:3], v[0:1], v[80:81] op_sel_hi:[0,1]
	v_cvt_pk_f16_f32 v9, v2, v3
	v_pk_add_f32 v[2:3], v[0:1], v[70:71] op_sel_hi:[0,1]
	s_nop 0
	s_waitcnt lgkmcnt(3)
	v_mfma_f32_16x16x32_f16 a[0:3], v[6:9], v[144:147], a[0:3]
	ds_read_b128 v[144:147], v124 offset:45072
	s_nop 0
	s_waitcnt lgkmcnt(3)
	v_mfma_f32_16x16x32_f16 a[4:7], v[6:9], v[148:151], a[4:7]
	ds_read_b128 v[148:151], v124 offset:58384
	v_cvt_pk_f16_f32 v6, v2, v3
	v_pk_add_f32 v[2:3], v[0:1], v[72:73] op_sel_hi:[0,1]
	v_cvt_pk_f16_f32 v7, v2, v3
	v_pk_add_f32 v[2:3], v[0:1], v[82:83] op_sel_hi:[0,1]
	v_cvt_pk_f16_f32 v8, v2, v3
	v_pk_add_f32 v[2:3], v[0:1], v[84:85] op_sel_hi:[0,1]
	v_cvt_pk_f16_f32 v9, v2, v3
	v_pk_add_f32 v[2:3], v[0:1], v[90:91] op_sel_hi:[0,1]
	s_nop 0
	s_waitcnt lgkmcnt(3)
	v_mfma_f32_16x16x32_f16 a[0:3], v[6:9], v[152:155], a[0:3]
	ds_read_b128 v[152:155], v124 offset:46096
	s_nop 0
	s_waitcnt lgkmcnt(3)
	v_mfma_f32_16x16x32_f16 a[4:7], v[6:9], v[156:159], a[4:7]
	ds_read_b128 v[156:159], v124 offset:59408
	v_cvt_pk_f16_f32 v6, v2, v3
	v_pk_add_f32 v[2:3], v[0:1], v[92:93] op_sel_hi:[0,1]
	v_cvt_pk_f16_f32 v7, v2, v3
	v_pk_add_f32 v[2:3], v[0:1], v[94:95] op_sel_hi:[0,1]
	v_cvt_pk_f16_f32 v8, v2, v3
	v_pk_add_f32 v[2:3], v[0:1], v[96:97] op_sel_hi:[0,1]
	v_cvt_pk_f16_f32 v9, v2, v3
	v_pk_add_f32 v[2:3], v[0:1], v[86:87] op_sel_hi:[0,1]
	s_nop 0
	s_waitcnt lgkmcnt(3)
	v_mfma_f32_16x16x32_f16 a[0:3], v[6:9], v[144:147], a[0:3]
	ds_read_b128 v[144:147], v124 offset:47120
	s_nop 0
	s_waitcnt lgkmcnt(3)
	v_mfma_f32_16x16x32_f16 a[4:7], v[6:9], v[148:151], a[4:7]
	ds_read_b128 v[148:151], v124 offset:60432
	v_cvt_pk_f16_f32 v6, v2, v3
	v_pk_add_f32 v[2:3], v[0:1], v[88:89] op_sel_hi:[0,1]
	v_cvt_pk_f16_f32 v7, v2, v3
	v_pk_add_f32 v[2:3], v[0:1], v[98:99] op_sel_hi:[0,1]
	v_pk_add_f32 v[0:1], v[0:1], v[100:101] op_sel_hi:[0,1]
	v_cvt_pk_f16_f32 v8, v2, v3
	v_cvt_pk_f16_f32 v9, v0, v1
	v_mov_b32_e32 v0, 0x180
	s_nop 0
	s_waitcnt lgkmcnt(3)
	v_mfma_f32_16x16x32_f16 a[128:131], v[6:9], v[152:155], a[0:3]
	v_lshl_or_b32 v0, v114, 3, v0
	v_cmp_gt_u32_e64 s[2:3], s2, v0
	s_and_b64 s[2:3], vcc, s[2:3]
	s_nop 0
	s_waitcnt lgkmcnt(2)
	v_mfma_f32_16x16x32_f16 a[0:3], v[6:9], v[156:159], a[4:7]
	v_cndmask_b32_e64 v0, 0, 1.0, s[2:3]
	v_pk_add_f32 v[2:3], v[0:1], v[106:107] op_sel_hi:[0,1]
	v_cvt_pk_f16_f32 v6, v2, v3
	v_pk_add_f32 v[2:3], v[0:1], v[108:109] op_sel_hi:[0,1]
	v_cvt_pk_f16_f32 v7, v2, v3
	v_pk_add_f32 v[2:3], v[0:1], v[102:103] op_sel_hi:[0,1]
	v_pk_add_f32 v[0:1], v[0:1], v[104:105] op_sel_hi:[0,1]
	v_cvt_pk_f16_f32 v8, v2, v3
	v_cvt_pk_f16_f32 v9, v0, v1
	v_mov_b32_e32 v0, 0x27010
	s_nop 0
	s_waitcnt lgkmcnt(1)
	v_mfma_f32_16x16x32_f16 a[4:7], v[6:9], v[144:147], a[128:131]
	s_nop 0
	s_waitcnt lgkmcnt(0)
	v_mfma_f32_16x16x32_f16 a[0:3], v[6:9], v[148:151], a[0:3]
	s_nop 6
	v_accvgpr_read_b32 v13, a7
	v_accvgpr_read_b32 v10, a4
	v_lshlrev_b32_e32 v10, 2, v114
	v_or_b32_e32 v14, 1, v10
	v_accvgpr_read_b32 v12, a6
	v_accvgpr_read_b32 v11, a5
	v_cmp_gt_u32_e32 vcc, 13, v14
	v_accvgpr_read_b32 v9, a3
	v_accvgpr_read_b32 v6, a0
	v_lshl_add_u32 v6, v183, 2, v0
	v_accvgpr_read_b32 v8, a2
	v_accvgpr_read_b32 v7, a1
	v_lshl_add_u32 v0, v114, 9, v6
	ds_write_b32 v0, a4
	ds_write_b32 v0, a0 offset:64
	s_and_saveexec_b64 s[2:3], vcc
	v_lshl_add_u32 v0, v14, 7, v6
	ds_write2_b32 v0, v11, v7 offset1:16
	s_or_b64 exec, exec, s[2:3]
	v_or_b32_e32 v7, 2, v10
	v_cmp_gt_u32_e32 vcc, 13, v7
	s_and_saveexec_b64 s[2:3], vcc
	v_lshl_add_u32 v0, v7, 7, v6
	ds_write2_b32 v0, v12, v8 offset1:16
	s_or_b64 exec, exec, s[2:3]
	v_or_b32_e32 v7, 3, v10
	v_cmp_gt_u32_e32 vcc, 13, v7
	s_and_b64 exec, exec, vcc
	v_lshl_add_u32 v0, v7, 7, v6
	ds_write2_b32 v0, v13, v9 offset1:16
